# baseline (speedup 1.0000x reference)
_Z9k3_reducePKfPf:
	v_and_b32_e32 v1, 63, v0
	s_load_dwordx2 s[4:5], s[0:1], 0x0
	v_lshl_or_b32 v2, s2, 6, v1
	s_mov_b32 s2, 0xea0ea0eb
	v_mul_hi_i32 v1, v2, s2
	v_add_u32_e32 v1, v1, v2
	v_lshrrev_b32_e32 v3, 31, v1
	v_ashrrev_i32_e32 v1, 11, v1
	v_lshrrev_b32_e32 v5, 1, v0
	v_add_u32_e32 v1, v1, v3
	s_movk_i32 s2, 0xf740
	v_and_b32_e32 v5, 0x60, v5
	v_mad_i32_i24 v4, v1, s2, v2
	v_ashrrev_i32_e32 v3, 31, v1
	v_lshl_or_b32 v1, v1, 7, v5
	s_movk_i32 s6, 0x2300
	s_waitcnt lgkmcnt(0)
	v_mov_b64_e32 v[6:7], s[4:5]
	v_mad_u64_u32 v[6:7], s[2:3], v1, s6, v[6:7]
	v_mad_i32_i24 v7, v3, s6, v7
	v_ashrrev_i32_e32 v5, 31, v4
	v_lshl_add_u64 v[4:5], v[4:5], 2, v[6:7]
	s_movk_i32 s2, 0x2000
	v_add_co_u32_e32 v6, vcc, s2, v4
	s_movk_i32 s2, 0x4000
	s_nop 0
	v_addc_co_u32_e32 v7, vcc, 0, v5, vcc
	v_add_co_u32_e32 v8, vcc, s2, v4
	s_movk_i32 s2, 0x6000
	s_nop 0
	v_addc_co_u32_e32 v9, vcc, 0, v5, vcc
	v_add_co_u32_e32 v10, vcc, s2, v4
	s_mov_b32 s2, 0x8000
	s_nop 0
	v_addc_co_u32_e32 v11, vcc, 0, v5, vcc
	v_add_co_u32_e32 v12, vcc, s2, v4
	s_mov_b32 s2, 0xa000
	s_nop 0
	v_addc_co_u32_e32 v13, vcc, 0, v5, vcc
	v_add_co_u32_e32 v14, vcc, s2, v4
	s_mov_b32 s2, 0xd000
	s_nop 0
	v_addc_co_u32_e32 v15, vcc, 0, v5, vcc
	v_add_co_u32_e32 v16, vcc, s2, v4
	s_mov_b32 s2, 0xf000
	s_nop 0
	v_addc_co_u32_e32 v17, vcc, 0, v5, vcc
	v_add_co_u32_e32 v18, vcc, s2, v4
	s_mov_b32 s2, 0x11000
	s_nop 0
	v_addc_co_u32_e32 v19, vcc, 0, v5, vcc
	global_load_dword v1, v[4:5], off
	global_load_dword v3, v[6:7], off offset:768
	global_load_dword v22, v[8:9], off offset:1536
	global_load_dword v23, v[10:11], off offset:2304
	global_load_dword v24, v[12:13], off offset:3072
	global_load_dword v25, v[14:15], off offset:3840
	global_load_dword v26, v[16:17], off offset:512
	global_load_dword v27, v[18:19], off offset:1280
	v_add_co_u32_e32 v6, vcc, s2, v4
	s_mov_b32 s2, 0x13000
	s_nop 0
	v_addc_co_u32_e32 v7, vcc, 0, v5, vcc
	v_add_co_u32_e32 v8, vcc, s2, v4
	s_mov_b32 s2, 0x15000
	s_nop 0
	v_addc_co_u32_e32 v9, vcc, 0, v5, vcc
	v_add_co_u32_e32 v10, vcc, s2, v4
	s_mov_b32 s2, 0x18000
	s_nop 0
	v_addc_co_u32_e32 v11, vcc, 0, v5, vcc
	v_add_co_u32_e32 v12, vcc, s2, v4
	s_mov_b32 s2, 0x1a000
	s_nop 0
	v_addc_co_u32_e32 v13, vcc, 0, v5, vcc
	v_add_co_u32_e32 v14, vcc, s2, v4
	s_mov_b32 s2, 0x1c000
	s_nop 0
	v_addc_co_u32_e32 v15, vcc, 0, v5, vcc
	v_add_co_u32_e32 v16, vcc, s2, v4
	s_mov_b32 s2, 0x1e000
	s_nop 0
	v_addc_co_u32_e32 v17, vcc, 0, v5, vcc
	v_add_co_u32_e32 v18, vcc, s2, v4
	s_mov_b32 s2, 0x20000
	s_nop 0
	v_addc_co_u32_e32 v19, vcc, 0, v5, vcc
	v_add_co_u32_e32 v20, vcc, s2, v4
	s_mov_b32 s2, 0x23000
	s_nop 0
	v_addc_co_u32_e32 v21, vcc, 0, v5, vcc
	global_load_dword v28, v[6:7], off offset:2048
	global_load_dword v29, v[8:9], off offset:2816
	global_load_dword v30, v[10:11], off offset:3584
	global_load_dword v31, v[12:13], off offset:256
	global_load_dword v32, v[14:15], off offset:1024
	global_load_dword v33, v[16:17], off offset:1792
	global_load_dword v34, v[18:19], off offset:2560
	global_load_dword v35, v[20:21], off offset:3328
	v_add_co_u32_e32 v6, vcc, s2, v4
	s_mov_b32 s2, 0x25000
	s_nop 0
	v_addc_co_u32_e32 v7, vcc, 0, v5, vcc
	v_add_co_u32_e32 v8, vcc, s2, v4
	s_mov_b32 s2, 0x27000
	s_nop 0
	v_addc_co_u32_e32 v9, vcc, 0, v5, vcc
	v_add_co_u32_e32 v10, vcc, s2, v4
	s_mov_b32 s2, 0x29000
	s_nop 0
	v_addc_co_u32_e32 v11, vcc, 0, v5, vcc
	v_add_co_u32_e32 v12, vcc, s2, v4
	s_mov_b32 s2, 0x2b000
	s_nop 0
	v_addc_co_u32_e32 v13, vcc, 0, v5, vcc
	v_add_co_u32_e32 v14, vcc, s2, v4
	s_mov_b32 s2, 0x2d000
	s_nop 0
	v_addc_co_u32_e32 v15, vcc, 0, v5, vcc
	v_add_co_u32_e32 v16, vcc, s2, v4
	s_mov_b32 s2, 0x30000
	s_nop 0
	v_addc_co_u32_e32 v17, vcc, 0, v5, vcc
	v_add_co_u32_e32 v18, vcc, s2, v4
	s_mov_b32 s2, 0x32000
	s_nop 0
	v_addc_co_u32_e32 v19, vcc, 0, v5, vcc
	v_add_co_u32_e32 v20, vcc, s2, v4
	s_mov_b32 s2, 0x34000
	s_nop 0
	v_addc_co_u32_e32 v21, vcc, 0, v5, vcc
	global_load_dword v36, v[6:7], off
	global_load_dword v37, v[8:9], off offset:768
	global_load_dword v38, v[10:11], off offset:1536
	global_load_dword v39, v[12:13], off offset:2304
	global_load_dword v40, v[14:15], off offset:3072
	global_load_dword v41, v[16:17], off offset:3840
	global_load_dword v42, v[18:19], off offset:512
	global_load_dword v43, v[20:21], off offset:1280
	v_add_co_u32_e32 v6, vcc, s2, v4
	s_mov_b32 s2, 0x36000
	s_nop 0
	v_addc_co_u32_e32 v7, vcc, 0, v5, vcc
	v_add_co_u32_e32 v8, vcc, s2, v4
	s_mov_b32 s2, 0x38000
	s_nop 0
	v_addc_co_u32_e32 v9, vcc, 0, v5, vcc
	v_add_co_u32_e32 v10, vcc, s2, v4
	s_mov_b32 s2, 0x3b000
	s_nop 0
	v_addc_co_u32_e32 v11, vcc, 0, v5, vcc
	v_add_co_u32_e32 v12, vcc, s2, v4
	s_mov_b32 s2, 0x3d000
	s_nop 0
	v_addc_co_u32_e32 v13, vcc, 0, v5, vcc
	v_add_co_u32_e32 v14, vcc, s2, v4
	s_mov_b32 s2, 0x3f000
	s_nop 0
	v_addc_co_u32_e32 v15, vcc, 0, v5, vcc
	v_add_co_u32_e32 v16, vcc, s2, v4
	s_mov_b32 s2, 0x41000
	s_nop 0
	v_addc_co_u32_e32 v17, vcc, 0, v5, vcc
	v_add_co_u32_e32 v18, vcc, s2, v4
	s_waitcnt vmcnt(23)
	v_add_f32_e32 v1, 0, v1
	v_addc_co_u32_e32 v19, vcc, 0, v5, vcc
	v_add_co_u32_e32 v4, vcc, 0x43000, v4
	s_waitcnt vmcnt(22)
	v_add_f32_e32 v1, v1, v3
	v_addc_co_u32_e32 v5, vcc, 0, v5, vcc
	global_load_dword v20, v[6:7], off offset:2048
	global_load_dword v21, v[8:9], off offset:2816
	global_load_dword v44, v[10:11], off offset:3584
	global_load_dword v45, v[12:13], off offset:256
	global_load_dword v46, v[14:15], off offset:1024
	global_load_dword v47, v[16:17], off offset:1792
	global_load_dword v48, v[18:19], off offset:2560
	global_load_dword v49, v[4:5], off offset:3328
	s_waitcnt vmcnt(29)
	v_add_f32_e32 v1, v1, v22
	s_waitcnt vmcnt(28)
	v_add_f32_e32 v1, v1, v23
	s_waitcnt vmcnt(27)
	v_add_f32_e32 v1, v1, v24
	s_waitcnt vmcnt(26)
	v_add_f32_e32 v1, v1, v25
	s_waitcnt vmcnt(25)
	v_add_f32_e32 v1, v1, v26
	s_waitcnt vmcnt(24)
	v_add_f32_e32 v1, v1, v27
	s_waitcnt vmcnt(23)
	v_add_f32_e32 v1, v1, v28
	s_waitcnt vmcnt(22)
	v_add_f32_e32 v1, v1, v29
	s_waitcnt vmcnt(21)
	v_add_f32_e32 v1, v1, v30
	s_waitcnt vmcnt(20)
	v_add_f32_e32 v1, v1, v31
	s_waitcnt vmcnt(19)
	v_add_f32_e32 v1, v1, v32
	s_waitcnt vmcnt(18)
	v_add_f32_e32 v1, v1, v33
	s_waitcnt vmcnt(17)
	v_add_f32_e32 v1, v1, v34
	s_waitcnt vmcnt(16)
	v_add_f32_e32 v1, v1, v35
	v_cmp_gt_u32_e32 vcc, 64, v0
	s_waitcnt vmcnt(15)
	v_add_f32_e32 v1, v1, v36
	s_waitcnt vmcnt(14)
	v_add_f32_e32 v1, v1, v37
	s_waitcnt vmcnt(13)
	v_add_f32_e32 v1, v1, v38
	s_waitcnt vmcnt(12)
	v_add_f32_e32 v1, v1, v39
	s_waitcnt vmcnt(11)
	v_add_f32_e32 v1, v1, v40
	s_waitcnt vmcnt(10)
	v_add_f32_e32 v1, v1, v41
	s_waitcnt vmcnt(9)
	v_add_f32_e32 v1, v1, v42
	s_waitcnt vmcnt(8)
	v_add_f32_e32 v1, v1, v43
	s_waitcnt vmcnt(7)
	v_add_f32_e32 v1, v1, v20
	s_waitcnt vmcnt(6)
	v_add_f32_e32 v1, v1, v21
	s_waitcnt vmcnt(5)
	v_add_f32_e32 v1, v1, v44
	s_waitcnt vmcnt(4)
	v_add_f32_e32 v1, v1, v45
	s_waitcnt vmcnt(3)
	v_add_f32_e32 v1, v1, v46
	s_waitcnt vmcnt(2)
	v_add_f32_e32 v1, v1, v47
	s_waitcnt vmcnt(1)
	v_add_f32_e32 v1, v1, v48
	s_waitcnt vmcnt(0)
	v_add_f32_e32 v3, v1, v49
	v_lshlrev_b32_e32 v1, 2, v0
	ds_write_b32 v1, v3
	s_waitcnt lgkmcnt(0)
	s_barrier
	s_and_saveexec_b64 s[2:3], vcc
	s_cbranch_execz .LBB3_2
	ds_read2st64_b32 v[4:5], v1 offset1:1
	ds_read2st64_b32 v[0:1], v1 offset0:2 offset1:3
	s_load_dwordx2 s[0:1], s[0:1], 0x8
	v_ashrrev_i32_e32 v3, 31, v2
	s_waitcnt lgkmcnt(0)
	v_add_f32_e32 v4, v4, v5
	v_add_f32_e32 v0, v4, v0
	v_add_f32_e32 v4, v0, v1
	v_lshl_add_u64 v[0:1], v[2:3], 2, s[0:1]
	global_store_dword v[0:1], v4, off
